# baseline (speedup 1.0000x reference)
.Lattn_g_done:
	s_and_saveexec_b64 s[40:41], s[0:1]
	s_cbranch_execz .LBB0_108
	s_setprio 2
	v_mov_b32_e32 v2, v54
	s_waitcnt vmcnt(5)
	v_mov_b32_e32 v99, v112
	v_permlane16_swap_b32_e32 v2, v54
	v_mov_b32_e32 v100, v113
	v_mov_b32_e32 v101, v114
	v_add_f32_e32 v54, v54, v2
	v_mov_b32_e32 v55, v54
	v_mov_b32_e32 v102, v115
	s_nop 0
	v_permlane32_swap_b32_e32 v55, v54
	s_lshl_b32 s95, s80, 1
	v_mov_b32_e32 v2, s95
	v_or_b32_e32 v4, 1, v2
	v_cmp_gt_i32_e32 vcc, s33, v4
	ds_read_b128 v[4:7], v86 offset:32768
	ds_read_b128 v[8:11], v86 offset:33792
	ds_read_b128 v[12:15], v86 offset:34816
	ds_read_b128 v[16:19], v86 offset:35840
	v_cvt_pk_f16_f32 v53, v52, v53
	v_cvt_pk_f16_f32 v52, v50, v51
	v_cvt_pk_f16_f32 v51, v48, v49
	v_cvt_pk_f16_f32 v50, v46, v47
	v_cvt_pk_f16_f32 v45, v44, v45
	v_cvt_pk_f16_f32 v44, v42, v43
	v_cvt_pk_f16_f32 v43, v40, v41
	v_cvt_pk_f16_f32 v42, v38, v39
	v_cvt_pk_f16_f32 v37, v36, v37
	v_cvt_pk_f16_f32 v36, v34, v35
	v_cvt_pk_f16_f32 v35, v32, v33
	v_cvt_pk_f16_f32 v34, v30, v31
	ds_read_b128 v[30:33], v86 offset:36864
	ds_read_b128 v[38:41], v86 offset:37888
	ds_read_b128 v[46:49], v86 offset:38912
	ds_read_b128 v[56:59], v86 offset:39936
	v_cvt_pk_f16_f32 v63, v28, v29
	v_cvt_pk_f16_f32 v62, v26, v27
	v_cvt_pk_f16_f32 v61, v24, v25
	v_cvt_pk_f16_f32 v60, v22, v23
	s_waitcnt lgkmcnt(7)
	v_mfma_f32_16x16x32_f16 v[4:7], v[4:7], v[50:53], 0
	s_waitcnt lgkmcnt(6)
	v_mfma_f32_16x16x32_f16 v[4:7], v[8:11], v[42:45], v[4:7]
	s_waitcnt lgkmcnt(5)
	v_mfma_f32_16x16x32_f16 v[4:7], v[12:15], v[34:37], v[4:7]
	s_waitcnt lgkmcnt(4)
	v_mfma_f32_16x16x32_f16 v[12:15], v[16:19], v[60:63], v[4:7]
	ds_read_b128 v[8:11], v86 offset:44032
	ds_read_b128 v[16:19], v86 offset:43008
	ds_read_b128 v[20:23], v86 offset:41984
	ds_read_b128 v[24:27], v86 offset:40960
	s_waitcnt lgkmcnt(7)
	v_mfma_f32_16x16x32_f16 v[4:7], v[30:33], v[50:53], 0
	s_waitcnt lgkmcnt(6)
	v_mfma_f32_16x16x32_f16 v[4:7], v[38:41], v[42:45], v[4:7]
	s_waitcnt lgkmcnt(5)
	v_mfma_f32_16x16x32_f16 v[4:7], v[46:49], v[34:37], v[4:7]
	s_waitcnt lgkmcnt(4)
	v_mfma_f32_16x16x32_f16 v[4:7], v[56:59], v[60:63], v[4:7]
	ds_read_b128 v[28:31], v86 offset:45056
	ds_read_b128 v[38:41], v86 offset:46080
	ds_read_b128 v[46:49], v86 offset:47104
	ds_read_b128 v[56:59], v86 offset:48128
	s_waitcnt lgkmcnt(4)
	v_mfma_f32_16x16x32_f16 v[24:27], v[24:27], v[50:53], 0
	v_mfma_f32_16x16x32_f16 v[20:23], v[20:23], v[42:45], v[24:27]
	v_mfma_f32_16x16x32_f16 v[16:19], v[16:19], v[34:37], v[20:23]
	v_mfma_f32_16x16x32_f16 v[8:11], v[8:11], v[60:63], v[16:19]
	s_nop 5
	ds_read_b128 v[20:23], v86 offset:52224
	ds_read_b128 v[24:27], v86 offset:51200
	ds_read_b128 v[64:67], v86 offset:50176
	ds_read_b128 v[104:107], v86 offset:49152
	s_waitcnt lgkmcnt(7)
	v_mfma_f32_16x16x32_f16 v[16:19], v[28:31], v[50:53], 0
	s_waitcnt lgkmcnt(6)
	v_mfma_f32_16x16x32_f16 v[16:19], v[38:41], v[42:45], v[16:19]
	s_waitcnt lgkmcnt(5)
	v_mfma_f32_16x16x32_f16 v[16:19], v[46:49], v[34:37], v[16:19]
	s_waitcnt lgkmcnt(4)
	v_mfma_f32_16x16x32_f16 v[16:19], v[56:59], v[60:63], v[16:19]
	ds_read_b128 v[28:31], v86 offset:53248
	ds_read_b128 v[38:41], v86 offset:54272
	ds_read_b128 v[46:49], v86 offset:55296
	ds_read_b128 v[56:59], v86 offset:56320
	s_waitcnt lgkmcnt(4)
	v_mfma_f32_16x16x32_f16 v[104:107], v[104:107], v[50:53], 0
	v_mfma_f32_16x16x32_f16 v[64:67], v[64:67], v[42:45], v[104:107]
	v_mfma_f32_16x16x32_f16 v[24:27], v[24:27], v[34:37], v[64:67]
	v_mfma_f32_16x16x32_f16 v[20:23], v[20:23], v[60:63], v[24:27]
	s_nop 5
	ds_read_b128 v[64:67], v86 offset:60416
	ds_read_b128 v[104:107], v86 offset:59392
	ds_read_b128 v[108:111], v86 offset:58368
	ds_read_b128 v[112:115], v86 offset:57344
	s_waitcnt lgkmcnt(7)
	v_mfma_f32_16x16x32_f16 v[24:27], v[28:31], v[50:53], 0
	s_waitcnt lgkmcnt(6)
	v_mfma_f32_16x16x32_f16 v[24:27], v[38:41], v[42:45], v[24:27]
	s_waitcnt lgkmcnt(5)
	v_mfma_f32_16x16x32_f16 v[24:27], v[46:49], v[34:37], v[24:27]
	s_waitcnt lgkmcnt(4)
	v_mfma_f32_16x16x32_f16 v[24:27], v[56:59], v[60:63], v[24:27]
	ds_read_b128 v[38:41], v86 offset:61440
	ds_read_b128 v[46:49], v86 offset:62464
	ds_read_b128 v[56:59], v86 offset:63488
	ds_read_b128 v[116:119], v86 offset:64512
	s_waitcnt lgkmcnt(4)
	v_mfma_f32_16x16x32_f16 v[28:31], v[112:115], v[50:53], 0
	v_mfma_f32_16x16x32_f16 v[28:31], v[108:111], v[42:45], v[28:31]
	v_mfma_f32_16x16x32_f16 v[28:31], v[104:107], v[34:37], v[28:31]
	v_mfma_f32_16x16x32_f16 v[28:31], v[64:67], v[60:63], v[28:31]
	s_waitcnt lgkmcnt(3)
	v_mfma_f32_16x16x32_f16 v[38:41], v[38:41], v[50:53], 0
	s_waitcnt lgkmcnt(2)
	v_mfma_f32_16x16x32_f16 v[38:41], v[46:49], v[42:45], v[38:41]
	s_waitcnt lgkmcnt(1)
	v_mfma_f32_16x16x32_f16 v[32:35], v[56:59], v[34:37], v[38:41]
	s_waitcnt lgkmcnt(0)
	v_mfma_f32_16x16x32_f16 v[32:35], v[116:119], v[60:63], v[32:35]
	s_or_b64 s[42:43], s[38:39], vcc
	s_and_saveexec_b64 s[0:1], s[42:43]
	s_cbranch_execz .LBB0_105
	v_lshlrev_b32_e32 v36, 1, v78
	ds_read_b128 v[36:39], v36 offset:27472
	v_cndmask_b32_e64 v12, 0, v12, s[14:15]
	v_cndmask_b32_e64 v13, 0, v13, s[14:15]
	v_cndmask_b32_e64 v14, 0, v14, s[14:15]
	v_cndmask_b32_e64 v15, 0, v15, s[14:15]
	v_cndmask_b32_e64 v7, v15, v7, s[12:13]
	v_cndmask_b32_e64 v6, v14, v6, s[12:13]
	v_cndmask_b32_e64 v5, v13, v5, s[12:13]
	v_cndmask_b32_e64 v4, v12, v4, s[12:13]
	v_add_f32_e32 v40, v54, v55
	v_cndmask_b32_e64 v4, v4, v8, s[10:11]
	v_cndmask_b32_e64 v5, v5, v9, s[10:11]
	v_cndmask_b32_e64 v6, v6, v10, s[10:11]
	v_cndmask_b32_e64 v7, v7, v11, s[10:11]
	v_rcp_f32_e32 v12, v40
	v_cndmask_b32_e64 v7, v7, v19, s[8:9]
	v_cndmask_b32_e64 v6, v6, v18, s[8:9]
	v_cndmask_b32_e64 v5, v5, v17, s[8:9]
	v_cndmask_b32_e64 v4, v4, v16, s[8:9]
	v_cndmask_b32_e64 v4, v4, v20, s[6:7]
	v_cndmask_b32_e64 v5, v5, v21, s[6:7]
	v_cndmask_b32_e64 v6, v6, v22, s[6:7]
	v_cndmask_b32_e64 v7, v7, v23, s[6:7]
	v_cndmask_b32_e64 v7, v7, v27, s[20:21]
	v_cndmask_b32_e64 v6, v6, v26, s[20:21]
	v_cndmask_b32_e64 v5, v5, v25, s[20:21]
	v_cndmask_b32_e64 v4, v4, v24, s[20:21]
	v_cmp_lt_f32_e32 vcc, 0, v40
	v_cndmask_b32_e64 v4, v4, v28, s[18:19]
	v_cndmask_b32_e64 v5, v5, v29, s[18:19]
	v_cndmask_b32_e64 v6, v6, v30, s[18:19]
	v_cndmask_b32_e64 v7, v7, v31, s[18:19]
	v_cndmask_b32_e32 v8, 0, v12, vcc
	v_cndmask_b32_e64 v7, v7, v35, s[16:17]
	v_cndmask_b32_e64 v6, v6, v34, s[16:17]
	v_cndmask_b32_e64 v5, v5, v33, s[16:17]
	v_cndmask_b32_e64 v4, v4, v32, s[16:17]
	v_or_b32_e32 v2, v2, v89
	s_waitcnt lgkmcnt(0)
	v_fma_mixlo_f16 v4, v8, v4, v36
	v_fma_mixlo_f16 v5, v8, v5, v37
	v_fma_mixlo_f16 v6, v8, v6, v38
	v_fma_mixlo_f16 v7, v8, v7, v39
	v_cndmask_b32_e32 v4, 0, v4, vcc
	v_cndmask_b32_e32 v8, 0, v5, vcc
	v_cndmask_b32_e32 v5, 0, v6, vcc
	v_cndmask_b32_e32 v6, 0, v7, vcc
	v_pack_b32_f16 v5, v5, v6
	v_pack_b32_f16 v4, v4, v8
	v_mad_u64_u32 v[6:7], s[42:43], v2, s72, v[78:79]
	ds_write_b64 v6, v[4:5]

.LBB0_107:
	s_or_b64 exec, exec, s[0:1]
	s_setprio 0
	v_mov_b32_e32 v5, 0xf149f2ca
	v_mov_b32_e32 v54, 0
